# wave-wide sums in norm1+dt-projection (P1) and layer-0 combine: 6-hop ds_bpermute butterflies replaced by DPP row ops + v_permlane16/32_swap (bit-identical)
# speedup vs baseline: 1.0551x; 1.0095x over previous
; __device__ __forceinline__ uint2 pack4(const f32x4 v) { uint2 o; o.x = pk2bf(v[0], v[1]); o.y = pk2bf(v[2], v[3]); return o; }
; __device__ __forceinline__ float wave_sum(float v) {
; #pragma unroll
;     for (int o = 1; o < 64; o <<= 1) v += __shfl_xor(v, o);
;     return v;
; }
; __device__ __forceinline__ void ph_norm1(const Ctx& c, int layer, int gw, int nwaves, unsigned char* lds) {
;     ...
;     for (int n = gw; n < NT; n += nwaves) {
;         const int b = n / LT, pos = n % LT, mr = pos < CTX ? 4 : b;
;         const float* x = xsrc(c, layer, n);
;         f32x4 v[4], sc[4], sh[4]; float ss = 0.f;
; #pragma unroll
;         for (int i = 0; i < 4; ++i) { const int k = (lane + 64 * i) * 4; v[i] = *(const f32x4*)(x + k); sc[i] = *(const f32x4*)(MOD + mr * 6144 + 1024 + k); sh[i] = *(const f32x4*)(MOD + mr * 6144 + k); }
; #pragma unroll
;         for (int i = 0; i < 4; ++i) ss += v[i][0] * v[i][0] + v[i][1] * v[i][1] + v[i][2] * v[i][2] + v[i][3] * v[i][3];
;         const float rstd = rsqrtf(wave_sum(ss) * (1.f / D) + EPS);
; #pragma unroll
;         for (int i = 0; i < 4; ++i) {
;             const int k = (lane + 64 * i) * 4;
;             v[i] = v[i] * rstd * gv[i] * (sc[i] + 1.f) + sh[i];
;             *(uint2*)(HA + (size_t)n * D + k) = pack4(v[i]);
;         }
;         dt_project(wdt, v, lane, DTR + (size_t)n * 8);
.LBB0_18:
	s_mov_b32 s0, 0x78787879
	v_mul_hi_i32 v2, v20, s0
	v_lshrrev_b32_e32 v21, 31, v2
	v_ashrrev_i32_e32 v2, 11, v2
	v_add_u32_e32 v34, v2, v21
	v_mul_i32_i24_e32 v2, 0x1100, v34
	v_sub_u32_e32 v21, v20, v2
	s_movk_i32 s0, 0x100
	v_cmp_gt_i32_e64 s[0:1], s0, v21
	v_ashrrev_i32_e32 v35, 31, v34
	v_add_u32_e32 v38, 0xffffff00, v21
	v_cndmask_b32_e64 v2, 0, 16, s[0:1]
	v_lshl_add_u64 v[36:37], s[4:5], 0, v[2:3]
	global_load_dwordx2 v[36:37], v[36:37], off
	v_cndmask_b32_e64 v2, 24, 20, s[0:1]
	v_lshlrev_b64 v[40:41], v2, v[34:35]
	v_mul_i32_i24_e32 v2, 0x1800, v34
	v_ashrrev_i32_e32 v39, 31, v21
	v_cndmask_b32_e64 v34, v2, v235, s[0:1]
	v_cndmask_b32_e64 v39, 0, v39, s[0:1]
	v_cndmask_b32_e64 v38, v38, v21, s[0:1]
	v_ashrrev_i32_e32 v35, 31, v34
	v_lshlrev_b64 v[38:39], 12, v[38:39]
	v_lshl_add_u64 v[42:43], v[34:35], 2, s[44:45]
	s_mov_b64 s[0:1], 0x1000
	v_lshl_add_u64 v[82:83], v[42:43], 0, s[0:1]
	v_lshl_add_u64 v[86:87], v[42:43], 0, v[26:27]
	v_lshl_add_u64 v[58:59], v[82:83], 0, v[28:29]
	v_lshl_add_u64 v[70:71], v[82:83], 0, v[30:31]
	s_mov_b32 s6, 0
	s_waitcnt vmcnt(0)
	v_lshl_add_u64 v[36:37], v[36:37], 0, v[40:41]
	v_lshl_add_u64 v[36:37], v[36:37], 0, v[38:39]
	v_lshl_add_u64 v[78:79], v[36:37], 0, v[26:27]
	v_lshl_add_u64 v[38:39], v[82:83], 0, v[26:27]
	global_load_dwordx4 v[34:37], v[78:79], off
	v_lshl_add_u64 v[82:83], v[82:83], 0, v[32:33]
	global_load_dwordx4 v[38:41], v[38:39], off
	s_nop 0
	global_load_dwordx4 v[42:45], v[86:87], off
	global_load_dwordx4 v[46:49], v[78:79], off offset:1024
	s_nop 0
	global_load_dwordx4 v[58:61], v[58:59], off
	s_nop 0
	global_load_dwordx4 v[62:65], v[86:87], off offset:1024
	global_load_dwordx4 v[66:69], v[78:79], off offset:2048
	s_nop 0
	global_load_dwordx4 v[70:73], v[70:71], off
	s_nop 0
	global_load_dwordx4 v[74:77], v[86:87], off offset:2048
	s_nop 0
	global_load_dwordx4 v[78:81], v[78:79], off offset:3072
	s_nop 0
	global_load_dwordx4 v[82:85], v[82:83], off
	s_nop 0
	global_load_dwordx4 v[86:89], v[86:87], off offset:3072
	s_waitcnt vmcnt(11)
	v_mov_b32_e32 v92, v35
	v_mov_b32_e32 v90, v34
	s_waitcnt vmcnt(10)
	v_pk_add_f32 v[38:39], v[38:39], 1.0 op_sel_hi:[1,0]
	s_waitcnt vmcnt(8)
	v_mov_b32_e32 v93, v47
	v_mov_b32_e32 v91, v46
	v_pk_mul_f32 v[92:93], v[92:93], v[92:93]
	s_waitcnt vmcnt(5)
	v_mov_b32_e32 v94, v67
	v_pk_fma_f32 v[90:91], v[90:91], v[90:91], v[92:93]
	v_mov_b32_e32 v92, v36
	v_mov_b32_e32 v93, v48
	v_pk_fma_f32 v[90:91], v[92:93], v[92:93], v[90:91]
	v_mov_b32_e32 v92, v37
	v_mov_b32_e32 v93, v49
	s_waitcnt vmcnt(2)
	v_mov_b32_e32 v95, v79
	v_pk_fma_f32 v[90:91], v[92:93], v[92:93], v[90:91]
	v_mov_b32_e32 v92, v66
	v_mov_b32_e32 v93, v78
	v_pk_mul_f32 v[94:95], v[94:95], v[94:95]
	v_add_f32_e32 v2, v90, v91
	v_pk_fma_f32 v[92:93], v[92:93], v[92:93], v[94:95]
	v_mov_b32_e32 v94, v68
	v_mov_b32_e32 v95, v80
	v_pk_fma_f32 v[92:93], v[94:95], v[94:95], v[92:93]
	v_mov_b32_e32 v94, v69
	v_mov_b32_e32 v95, v81
	v_pk_fma_f32 v[92:93], v[94:95], v[94:95], v[92:93]
	s_nop 0
	v_add_f32_e32 v2, v2, v92
	v_add_f32_e32 v2, v2, v93
	s_waitcnt lgkmcnt(0)
	s_nop 1
	v_add_f32_dpp v2, v2, v2 quad_perm:[1,0,3,2] row_mask:0xf bank_mask:0xf
	s_nop 1
	v_add_f32_dpp v2, v2, v2 quad_perm:[2,3,0,1] row_mask:0xf bank_mask:0xf
	s_nop 1
	v_add_f32_dpp v2, v2, v2 row_half_mirror row_mask:0xf bank_mask:0xf
	s_nop 1
	v_add_f32_dpp v2, v2, v2 row_mirror row_mask:0xf bank_mask:0xf
	v_mov_b32_e32 v21, v2
	s_nop 1
	v_permlane16_swap_b32_e32 v2, v21
	v_add_f32_e32 v2, v2, v21
	v_mov_b32_e32 v21, v2
	s_nop 1
	v_permlane32_swap_b32_e32 v2, v21
	v_add_f32_e32 v2, v2, v21
	v_fmamk_f32 v2, v2, 0x3a800000, v220
	v_cmp_gt_f32_e64 s[0:1], s91, v2
	v_mul_f32_e32 v21, 0x4b800000, v2
	s_nop 0
	v_cndmask_b32_e64 v2, v2, v21, s[0:1]
	v_rsq_f32_e32 v2, v2
	s_nop 0
	v_mul_f32_e32 v21, 0x45800000, v2
	v_cndmask_b32_e64 v2, v2, v21, s[0:1]
	v_pk_mul_f32 v[36:37], v[36:37], v[2:3] op_sel_hi:[1,0]
	v_pk_mul_f32 v[34:35], v[34:35], v[2:3] op_sel_hi:[1,0]
	v_ashrrev_i32_e32 v21, 31, v20
	v_pk_mul_f32 v[92:93], v[4:5], v[34:35]
	v_pk_mul_f32 v[34:35], v[6:7], v[36:37]
	v_pk_add_f32 v[36:37], v[40:41], 1.0 op_sel_hi:[1,0]
	v_lshlrev_b64 v[90:91], 11, v[20:21]
	v_pk_fma_f32 v[34:35], v[36:37], v[34:35], v[44:45]
	v_pk_fma_f32 v[92:93], v[38:39], v[92:93], v[42:43]
	v_cvt_pk_bf16_f32 v37, v34, v35
	v_cvt_pk_bf16_f32 v36, v92, v93
	v_lshl_add_u64 v[42:43], v[24:25], 0, v[90:91]
	global_store_dwordx2 v[42:43], v[36:37], off
	v_pk_mul_f32 v[36:37], v[48:49], v[2:3] op_sel_hi:[1,0]
	v_pk_mul_f32 v[38:39], v[46:47], v[2:3] op_sel_hi:[1,0]
	v_pk_mul_f32 v[36:37], v[10:11], v[36:37]
	v_pk_mul_f32 v[38:39], v[8:9], v[38:39]
	v_pk_add_f32 v[40:41], v[60:61], 1.0 op_sel_hi:[1,0]
	v_pk_add_f32 v[44:45], v[58:59], 1.0 op_sel_hi:[1,0]
	v_pk_fma_f32 v[48:49], v[40:41], v[36:37], v[64:65]
	v_pk_fma_f32 v[36:37], v[44:45], v[38:39], v[62:63]
	v_cvt_pk_bf16_f32 v39, v48, v49
	v_cvt_pk_bf16_f32 v38, v36, v37
	global_store_dwordx2 v[42:43], v[38:39], off offset:512
	v_pk_mul_f32 v[38:39], v[68:69], v[2:3] op_sel_hi:[1,0]
	v_pk_mul_f32 v[40:41], v[66:67], v[2:3] op_sel_hi:[1,0]
	v_pk_mul_f32 v[38:39], v[14:15], v[38:39]
	v_pk_mul_f32 v[40:41], v[12:13], v[40:41]
	v_pk_add_f32 v[44:45], v[72:73], 1.0 op_sel_hi:[1,0]
	v_pk_add_f32 v[46:47], v[70:71], 1.0 op_sel_hi:[1,0]
	v_pk_fma_f32 v[38:39], v[44:45], v[38:39], v[76:77]
	v_pk_fma_f32 v[46:47], v[46:47], v[40:41], v[74:75]
	v_cvt_pk_bf16_f32 v41, v38, v39
	v_cvt_pk_bf16_f32 v40, v46, v47
	global_store_dwordx2 v[42:43], v[40:41], off offset:1024
	v_pk_mul_f32 v[40:41], v[80:81], v[2:3] op_sel_hi:[1,0]
	v_pk_mul_f32 v[44:45], v[78:79], v[2:3] op_sel_hi:[1,0]
	v_pk_mul_f32 v[40:41], v[18:19], v[40:41]
	v_pk_mul_f32 v[44:45], v[16:17], v[44:45]
	s_waitcnt vmcnt(4)
	v_pk_add_f32 v[58:59], v[84:85], 1.0 op_sel_hi:[1,0]
	v_pk_add_f32 v[60:61], v[82:83], 1.0 op_sel_hi:[1,0]
	s_waitcnt vmcnt(3)
	v_pk_fma_f32 v[58:59], v[58:59], v[40:41], v[88:89]
	v_pk_fma_f32 v[40:41], v[60:61], v[44:45], v[86:87]
	v_cvt_pk_bf16_f32 v45, v58, v59
	v_cvt_pk_bf16_f32 v44, v40, v41
	global_store_dwordx2 v[42:43], v[44:45], off offset:1536
	v_mov_b32_e32 v42, v39
	v_mov_b32_e32 v43, v59
	v_mov_b32_e32 v39, v58
	v_mov_b32_e32 v44, v46
	v_mov_b32_e32 v45, v40
	v_mov_b32_e32 v40, v47
	v_mov_b32_e32 v46, v35
	v_mov_b32_e32 v47, v49
	v_mov_b32_e32 v35, v48
	v_mov_b32_e32 v48, v92
	v_mov_b32_e32 v49, v36
	v_mov_b32_e32 v36, v93
	v_mov_b32_e32 v58, 0
	v_mov_b32_e32 v2, v50
	v_mov_b32_e32 v59, v51
; #define LAS __attribute__((address_space(3)))
;     template <class T> __device__ __forceinline__ T* w(size_t off) const { return (T*)(p->ws + off); }
; __device__ __forceinline__ void dt_project(const LAS float* wdt, const f32x4 (&h)[4], int lane, float* dst) {
;     float mine = 0.f;
; #pragma unroll 2
;     for (int q = 0; q < 8; ++q) {
;         float s = 0.f;
; #pragma unroll
;         for (int i = 0; i < 4; ++i) { const f32x4 w = *(const LAS f32x4*)(wdt + q * 1024 + (lane + 64 * i) * 4); s += h[i][0] * w[0] + h[i][1] * w[1] + h[i][2] * w[2] + h[i][3] * w[3]; }
;         s = wave_sum(s);
;         if (lane == q) mine = s;
;     }
;     if (lane < 8) dst[lane] = mine;
; }
.LBB0_19:
	ds_read_b128 v[60:63], v59
	ds_read_b128 v[64:67], v59 offset:1024
	v_cmp_eq_u32_e64 s[0:1], 0, v2
	v_add_u32_e32 v2, -2, v2
	s_waitcnt lgkmcnt(1)
	v_mov_b32_e32 v68, v60
	s_waitcnt lgkmcnt(0)
	v_mov_b32_e32 v69, v64
	v_mov_b32_e32 v64, v61
	v_pk_mul_f32 v[60:61], v[36:37], v[64:65]
	v_mov_b32_e32 v64, v62
	v_pk_fma_f32 v[60:61], v[48:49], v[68:69], v[60:61]
	v_mov_b32_e32 v65, v66
	v_pk_fma_f32 v[60:61], v[34:35], v[64:65], v[60:61]
	v_mov_b32_e32 v66, v63
	v_pk_fma_f32 v[60:61], v[46:47], v[66:67], v[60:61]
	s_nop 0
	v_add_f32_e32 v60, 0, v60
	v_add_f32_e32 v70, v60, v61
	ds_read_b128 v[60:63], v59 offset:2048
	ds_read_b128 v[64:67], v59 offset:3072
	s_waitcnt lgkmcnt(1)
	v_mov_b32_e32 v68, v60
	s_waitcnt lgkmcnt(0)
	v_mov_b32_e32 v69, v64
	v_mov_b32_e32 v64, v61
	v_pk_mul_f32 v[60:61], v[40:41], v[64:65]
	v_mov_b32_e32 v64, v62
	v_pk_fma_f32 v[60:61], v[44:45], v[68:69], v[60:61]
	v_mov_b32_e32 v65, v66
	v_pk_fma_f32 v[60:61], v[38:39], v[64:65], v[60:61]
	v_mov_b32_e32 v66, v63
	v_pk_fma_f32 v[60:61], v[42:43], v[66:67], v[60:61]
	s_nop 0
	v_add_f32_e32 v60, v70, v60
	v_add_f32_e32 v60, v60, v61
	s_waitcnt lgkmcnt(0)
	s_nop 1
	v_add_f32_dpp v60, v60, v60 quad_perm:[1,0,3,2] row_mask:0xf bank_mask:0xf
	s_nop 1
	v_add_f32_dpp v60, v60, v60 quad_perm:[2,3,0,1] row_mask:0xf bank_mask:0xf
	s_nop 1
	v_add_f32_dpp v60, v60, v60 row_half_mirror row_mask:0xf bank_mask:0xf
	s_nop 1
	v_add_f32_dpp v60, v60, v60 row_mirror row_mask:0xf bank_mask:0xf
	v_mov_b32_e32 v61, v60
	s_nop 1
	v_permlane16_swap_b32_e32 v60, v61
	v_add_f32_e32 v60, v60, v61
	v_mov_b32_e32 v61, v60
	s_nop 1
	v_permlane32_swap_b32_e32 v60, v61
	v_add_f32_e32 v60, v60, v61
	v_cndmask_b32_e64 v58, v58, v60, s[0:1]
	ds_read_b128 v[60:63], v59 offset:4096
	ds_read_b128 v[64:67], v59 offset:5120
	s_or_b32 s0, s6, 1
	v_cmp_eq_u32_e64 s[0:1], s0, v50
	s_add_i32 s6, s6, 2
	s_waitcnt lgkmcnt(1)
	v_mov_b32_e32 v68, v60
	s_waitcnt lgkmcnt(0)
	v_mov_b32_e32 v69, v64
	v_mov_b32_e32 v64, v61
	v_pk_mul_f32 v[60:61], v[36:37], v[64:65]
	v_mov_b32_e32 v64, v62
	v_pk_fma_f32 v[60:61], v[48:49], v[68:69], v[60:61]
	v_mov_b32_e32 v65, v66
	v_pk_fma_f32 v[60:61], v[34:35], v[64:65], v[60:61]
	v_mov_b32_e32 v66, v63
	v_pk_fma_f32 v[60:61], v[46:47], v[66:67], v[60:61]
	s_cmp_lg_u32 s6, 8
	v_add_f32_e32 v60, 0, v60
	v_add_f32_e32 v70, v60, v61
	ds_read_b128 v[60:63], v59 offset:6144
	ds_read_b128 v[64:67], v59 offset:7168
	v_add_u32_e32 v59, 0x2000, v59
	s_waitcnt lgkmcnt(1)
	v_mov_b32_e32 v68, v60
	s_waitcnt lgkmcnt(0)
	v_mov_b32_e32 v69, v64
	v_mov_b32_e32 v64, v61
	v_pk_mul_f32 v[60:61], v[40:41], v[64:65]
	v_mov_b32_e32 v64, v62
	v_pk_fma_f32 v[60:61], v[44:45], v[68:69], v[60:61]
	v_mov_b32_e32 v65, v66
	v_pk_fma_f32 v[60:61], v[38:39], v[64:65], v[60:61]
	v_mov_b32_e32 v66, v63
	v_pk_fma_f32 v[60:61], v[42:43], v[66:67], v[60:61]
	s_nop 0
	v_add_f32_e32 v60, v70, v60
	v_add_f32_e32 v60, v60, v61
	s_waitcnt lgkmcnt(0)
	s_nop 1
	v_add_f32_dpp v60, v60, v60 quad_perm:[1,0,3,2] row_mask:0xf bank_mask:0xf
	s_nop 1
	v_add_f32_dpp v60, v60, v60 quad_perm:[2,3,0,1] row_mask:0xf bank_mask:0xf
	s_nop 1
	v_add_f32_dpp v60, v60, v60 row_half_mirror row_mask:0xf bank_mask:0xf
	s_nop 1
	v_add_f32_dpp v60, v60, v60 row_mirror row_mask:0xf bank_mask:0xf
	v_mov_b32_e32 v61, v60
	s_nop 1
	v_permlane16_swap_b32_e32 v60, v61
	v_add_f32_e32 v60, v60, v61
	v_mov_b32_e32 v61, v60
	s_nop 1
	v_permlane32_swap_b32_e32 v60, v61
	v_add_f32_e32 v60, v60, v61
	v_cndmask_b32_e64 v58, v58, v60, s[0:1]
	s_cbranch_scc1 .LBB0_19
	s_and_saveexec_b64 s[0:1], vcc
	s_cbranch_execz .LBB0_17
	v_lshlrev_b64 v[34:35], 5, v[20:21]
	v_lshl_add_u64 v[34:35], v[22:23], 0, v[34:35]
	global_store_dword v[34:35], v58, off
	s_branch .LBB0_17

; __device__ __forceinline__ f32x4 bf4(const uint2 u) { return (f32x4){__uint_as_float(u.x << 16), __uint_as_float(u.x & 0xffff0000u), __uint_as_float(u.y << 16), __uint_as_float(u.y & 0xffff0000u)}; }
; __device__ __forceinline__ void ph_combine(const Ctx& c, int layer, int bid, int G, const int* sm, unsigned char* lds) {
;     ...
;         for (int u = 0; u < 2; ++u) {
;             if (mr[u] != mrc) loadrow(mr[u]);
;             float ss = 0.f;
; #pragma unroll
;             for (int i = 0; i < 4; ++i) { xv[u][i] = xv[u][i] + G2c[i] * (bf4(oa[u][i]) * w0[u] + bf4(ob[u][i]) * w1[u]);
;                 ss += xv[u][i][0] * xv[u][i][0] + xv[u][i][1] * xv[u][i][1] + xv[u][i][2] * xv[u][i][2] + xv[u][i][3] * xv[u][i][3]; }
;             const float rstd = rsqrtf(wave_sum(ss) * (1.f / D) + EPS);
.LBB0_91:
	s_or_b64 exec, exec, s[28:29]
	v_cmp_lt_i32_e32 vcc, v229, v228
	s_waitcnt vmcnt(21)
	v_lshlrev_b32_e32 v16, 16, v214
	v_and_b32_e32 v17, 0xffff0000, v214
	v_cndmask_b32_e32 v12, v222, v229, vcc
	v_lshlrev_b32_e32 v114, 2, v12
	v_lshlrev_b32_e32 v12, 16, v212
	v_and_b32_e32 v13, 0xffff0000, v212
	v_pk_mul_f32 v[16:17], v[192:193], v[16:17] op_sel:[1,0]
	s_waitcnt vmcnt(20)
	v_lshlrev_b32_e32 v20, 16, v210
	v_and_b32_e32 v21, 0xffff0000, v210
	v_lshlrev_b32_e32 v18, 16, v215
	v_and_b32_e32 v19, 0xffff0000, v215
	v_pk_fma_f32 v[12:13], v[192:193], v[12:13], v[16:17] op_sel_hi:[0,1,1]
	v_lshlrev_b32_e32 v16, 16, v208
	v_and_b32_e32 v17, 0xffff0000, v208
	v_pk_mul_f32 v[20:21], v[192:193], v[20:21] op_sel:[1,0]
	v_lshlrev_b32_e32 v14, 16, v213
	v_and_b32_e32 v15, 0xffff0000, v213
	v_pk_mul_f32 v[18:19], v[192:193], v[18:19] op_sel:[1,0]
	v_lshlrev_b32_e32 v22, 16, v211
	v_and_b32_e32 v23, 0xffff0000, v211
	v_pk_fma_f32 v[16:17], v[192:193], v[16:17], v[20:21] op_sel_hi:[0,1,1]
	v_pk_fma_f32 v[14:15], v[192:193], v[14:15], v[18:19] op_sel_hi:[0,1,1]
	v_pk_fma_f32 v[12:13], v[12:13], v[54:55], v[106:107]
	v_lshlrev_b32_e32 v18, 16, v209
	v_and_b32_e32 v19, 0xffff0000, v209
	v_pk_mul_f32 v[22:23], v[192:193], v[22:23] op_sel:[1,0]
	v_pk_fma_f32 v[16:17], v[16:17], v[62:63], v[102:103]
	v_pk_fma_f32 v[18:19], v[192:193], v[18:19], v[22:23] op_sel_hi:[0,1,1]
	v_mov_b32_e32 v22, v13
	v_mov_b32_e32 v23, v17
	v_pk_fma_f32 v[14:15], v[14:15], v[56:57], v[108:109]
	v_pk_fma_f32 v[18:19], v[18:19], v[64:65], v[104:105]
	v_mov_b32_e32 v20, v12
	v_mov_b32_e32 v21, v16
	v_pk_mul_f32 v[22:23], v[22:23], v[22:23]
	s_waitcnt vmcnt(19)
	v_lshlrev_b32_e32 v24, 16, v206
	v_pk_fma_f32 v[20:21], v[20:21], v[20:21], v[22:23]
	v_mov_b32_e32 v22, v14
	v_mov_b32_e32 v23, v18
	v_pk_fma_f32 v[20:21], v[22:23], v[22:23], v[20:21]
	v_mov_b32_e32 v22, v15
	v_mov_b32_e32 v23, v19
	v_and_b32_e32 v25, 0xffff0000, v206
	v_pk_fma_f32 v[32:33], v[22:23], v[22:23], v[20:21]
	v_lshlrev_b32_e32 v20, 16, v204
	v_and_b32_e32 v21, 0xffff0000, v204
	v_pk_mul_f32 v[24:25], v[192:193], v[24:25] op_sel:[1,0]
	s_waitcnt vmcnt(18)
	v_lshlrev_b32_e32 v48, 16, v202
	v_and_b32_e32 v49, 0xffff0000, v202
	v_lshlrev_b32_e32 v26, 16, v207
	v_and_b32_e32 v27, 0xffff0000, v207
	v_pk_fma_f32 v[20:21], v[192:193], v[20:21], v[24:25] op_sel_hi:[0,1,1]
	v_lshlrev_b32_e32 v24, 16, v200
	v_and_b32_e32 v25, 0xffff0000, v200
	v_pk_mul_f32 v[48:49], v[192:193], v[48:49] op_sel:[1,0]
	v_lshlrev_b32_e32 v22, 16, v205
	v_and_b32_e32 v23, 0xffff0000, v205
	v_pk_mul_f32 v[26:27], v[192:193], v[26:27] op_sel:[1,0]
	v_lshlrev_b32_e32 v50, 16, v203
	v_and_b32_e32 v51, 0xffff0000, v203
	v_pk_fma_f32 v[24:25], v[192:193], v[24:25], v[48:49] op_sel_hi:[0,1,1]
	v_pk_fma_f32 v[22:23], v[192:193], v[22:23], v[26:27] op_sel_hi:[0,1,1]
	v_pk_fma_f32 v[20:21], v[20:21], v[70:71], v[98:99]
	v_lshlrev_b32_e32 v26, 16, v201
	v_and_b32_e32 v27, 0xffff0000, v201
	v_pk_mul_f32 v[50:51], v[192:193], v[50:51] op_sel:[1,0]
	v_pk_fma_f32 v[24:25], v[24:25], v[4:5], v[94:95]
	v_pk_fma_f32 v[26:27], v[192:193], v[26:27], v[50:51] op_sel_hi:[0,1,1]
	v_mov_b32_e32 v50, v21
	v_mov_b32_e32 v51, v25
	v_pk_fma_f32 v[22:23], v[22:23], v[72:73], v[100:101]
	v_pk_fma_f32 v[26:27], v[26:27], v[6:7], v[96:97]
	v_mov_b32_e32 v48, v20
	v_mov_b32_e32 v49, v24
	v_pk_mul_f32 v[50:51], v[50:51], v[50:51]
	v_add_f32_e32 v28, v32, v33
	v_pk_fma_f32 v[48:49], v[48:49], v[48:49], v[50:51]
	v_mov_b32_e32 v50, v22
	v_mov_b32_e32 v51, v26
	v_pk_fma_f32 v[48:49], v[50:51], v[50:51], v[48:49]
	v_mov_b32_e32 v50, v23
	v_mov_b32_e32 v51, v27
	v_pk_fma_f32 v[48:49], v[50:51], v[50:51], v[48:49]
	v_cmp_lt_i32_e32 vcc, v230, v228
	v_add_f32_e32 v28, v28, v48
	v_add_f32_e32 v28, v28, v49
	s_waitcnt lgkmcnt(0)
	s_nop 1
	v_add_f32_dpp v28, v28, v28 quad_perm:[1,0,3,2] row_mask:0xf bank_mask:0xf
	s_nop 1
	v_add_f32_dpp v28, v28, v28 quad_perm:[2,3,0,1] row_mask:0xf bank_mask:0xf
	s_nop 1
	v_add_f32_dpp v28, v28, v28 row_half_mirror row_mask:0xf bank_mask:0xf
	s_nop 1
	v_add_f32_dpp v28, v28, v28 row_mirror row_mask:0xf bank_mask:0xf
	v_mov_b32_e32 v32, v28
	s_nop 1
	v_permlane16_swap_b32_e32 v28, v32
	v_add_f32_e32 v28, v28, v32
	v_mov_b32_e32 v32, v28
	s_nop 1
	v_permlane32_swap_b32_e32 v28, v32
	v_add_f32_e32 v28, v28, v32
	v_cndmask_b32_e32 v33, v222, v230, vcc
	v_lshlrev_b32_e32 v107, 2, v33
	v_cmp_lt_i32_e32 vcc, v231, v228
	v_mov_b32_e32 v29, v118
	v_cndmask_b32_e32 v33, v222, v231, vcc
	v_lshlrev_b32_e32 v109, 2, v33
	v_cmp_lt_i32_e32 vcc, v232, v228
	s_mov_b64 s[6:7], -1
	v_cndmask_b32_e32 v33, v222, v232, vcc
	v_lshlrev_b32_e32 v115, 2, v33
	v_cmp_lt_i32_e32 vcc, v233, v228
	v_cndmask_b32_e32 v33, v222, v233, vcc
	v_lshlrev_b32_e32 v116, 2, v33
	v_cmp_lt_i32_e32 vcc, v234, v228
	v_cndmask_b32_e32 v33, v222, v234, vcc
	v_lshlrev_b32_e32 v117, 2, v33
	v_fmamk_f32 v28, v28, 0x3a800000, v220
	v_mul_f32_e32 v32, 0x4b800000, v28
	v_cmp_gt_f32_e32 vcc, s91, v28
	s_nop 1
	v_cndmask_b32_e32 v28, v28, v32, vcc
	v_rsq_f32_e32 v28, v28
	s_nop 0
	v_mul_f32_e32 v32, 0x45800000, v28
	v_cndmask_b32_e32 v28, v28, v32, vcc
	s_and_b64 vcc, exec, s[56:57]
	s_cbranch_vccz .LBB0_97
; #define LAS __attribute__((address_space(3)))
; __device__ __forceinline__ uint2 pack4(const f32x4 v) { uint2 o; o.x = pk2bf(v[0], v[1]); o.y = pk2bf(v[2], v[3]); return o; }
;     template <class T> __device__ __forceinline__ T* w(size_t off) const { return (T*)(p->ws + off); }
; __device__ __forceinline__ void dt_project(const LAS float* wdt, const f32x4 (&h)[4], int lane, float* dst) {
;     float mine = 0.f;
; #pragma unroll 2
;     for (int q = 0; q < 8; ++q) {
;         float s = 0.f;
; #pragma unroll
;         for (int i = 0; i < 4; ++i) { const f32x4 w = *(const LAS f32x4*)(wdt + q * 1024 + (lane + 64 * i) * 4); s += h[i][0] * w[0] + h[i][1] * w[1] + h[i][2] * w[2] + h[i][3] * w[3]; }
;         s = wave_sum(s);
;         if (lane == q) mine = s;
;     }
;     if (lane < 8) dst[lane] = mine;
; }
; __device__ __forceinline__ void ph_combine(const Ctx& c, int layer, int bid, int G, const int* sm, unsigned char* lds) {
;     ...
;             } else {
;                 float* X = c.w<float>(WS_X) + (size_t)n * D;
;                 f32x4 hv[4];
; #pragma unroll
;                 for (int i = 0; i < 4; ++i) {
;                     const int k = (lane + 64 * i) * 4;
;                     *(f32x4*)(X + k) = xv[u][i];
;                     hv[i] = xv[u][i] * rstd * GGc[i] + SSc[i];
;                     *(uint2*)(HA + (size_t)n * D + k) = pack4(hv[i]);
;                 }
;                 dt_project(wdt, hv, lane, DTR + (size_t)n * 8);
	v_pk_mul_f32 v[32:33], v[14:15], v[28:29] op_sel_hi:[1,0]
	v_pk_mul_f32 v[48:49], v[12:13], v[28:29] op_sel_hi:[1,0]
	v_pk_fma_f32 v[32:33], v[36:37], v[32:33], v[60:61]
	v_pk_fma_f32 v[104:105], v[38:39], v[48:49], v[58:59]
	v_lshlrev_b64 v[50:51], 11, v[190:191]
	v_cvt_pk_bf16_f32 v48, v104, v105
	v_cvt_pk_bf16_f32 v49, v32, v33
	v_lshl_add_u64 v[96:97], v[162:163], 0, v[50:51]
	global_store_dwordx4 v[198:199], v[12:15], off
	global_store_dwordx2 v[96:97], v[48:49], off
	global_store_dwordx4 v[198:199], v[16:19], off offset:1024
	v_pk_mul_f32 v[48:49], v[18:19], v[28:29] op_sel_hi:[1,0]
	v_pk_mul_f32 v[50:51], v[16:17], v[28:29] op_sel_hi:[1,0]
	v_pk_fma_f32 v[102:103], v[40:41], v[48:49], v[68:69]
	v_pk_fma_f32 v[48:49], v[42:43], v[50:51], v[66:67]
	v_cvt_pk_bf16_f32 v51, v102, v103
	v_cvt_pk_bf16_f32 v50, v48, v49
	global_store_dwordx2 v[96:97], v[50:51], off offset:512
	global_store_dwordx4 v[198:199], v[20:23], off offset:2048
	v_pk_mul_f32 v[50:51], v[22:23], v[28:29] op_sel_hi:[1,0]
	v_pk_mul_f32 v[94:95], v[20:21], v[28:29] op_sel_hi:[1,0]
	v_pk_fma_f32 v[50:51], v[30:31], v[50:51], v[76:77]
	v_pk_fma_f32 v[100:101], v[44:45], v[94:95], v[74:75]
	v_cvt_pk_bf16_f32 v95, v50, v51
	v_cvt_pk_bf16_f32 v94, v100, v101
	global_store_dwordx2 v[96:97], v[94:95], off offset:1024
	global_store_dwordx4 v[198:199], v[24:27], off offset:3072
	v_pk_mul_f32 v[94:95], v[26:27], v[28:29] op_sel_hi:[1,0]
	v_pk_mul_f32 v[98:99], v[24:25], v[28:29] op_sel_hi:[1,0]
	v_pk_fma_f32 v[110:111], v[34:35], v[94:95], v[10:11]
	v_pk_fma_f32 v[94:95], v[46:47], v[98:99], v[8:9]
	v_cvt_pk_bf16_f32 v99, v110, v111
	v_cvt_pk_bf16_f32 v98, v94, v95
	global_store_dwordx2 v[96:97], v[98:99], off offset:1536
	v_mov_b32_e32 v96, v51
	v_mov_b32_e32 v97, v111
	v_mov_b32_e32 v51, v110
	v_mov_b32_e32 v98, v100
	v_mov_b32_e32 v99, v94
	v_mov_b32_e32 v94, v101
	v_mov_b32_e32 v100, v33
	v_mov_b32_e32 v101, v103
	v_mov_b32_e32 v33, v102
	v_mov_b32_e32 v102, v104
	v_mov_b32_e32 v103, v48
	v_mov_b32_e32 v48, v105
	s_mov_b32 s6, 0
	v_mov_b32_e32 v106, 0
	v_mov_b32_e32 v104, v147
	v_mov_b32_e32 v105, v149
.LBB0_93:
	ds_read_b128 v[110:113], v105
	ds_read_b128 v[118:121], v105 offset:1024
	v_cmp_eq_u32_e32 vcc, 0, v104
	s_or_b32 s7, s6, 1
	s_add_i32 s6, s6, 2
	s_waitcnt lgkmcnt(1)
	v_mov_b32_e32 v192, v110
	s_waitcnt lgkmcnt(0)
	v_mov_b32_e32 v193, v118
	v_mov_b32_e32 v118, v111
	v_pk_mul_f32 v[110:111], v[48:49], v[118:119]
	v_mov_b32_e32 v118, v112
	v_pk_fma_f32 v[110:111], v[102:103], v[192:193], v[110:111]
	v_mov_b32_e32 v119, v120
	v_pk_fma_f32 v[110:111], v[32:33], v[118:119], v[110:111]
	v_mov_b32_e32 v120, v113
	v_pk_fma_f32 v[110:111], v[100:101], v[120:121], v[110:111]
	v_add_u32_e32 v104, -2, v104
	v_add_f32_e32 v108, 0, v110
	v_add_f32_e32 v108, v108, v111
	ds_read_b128 v[110:113], v105 offset:2048
	ds_read_b128 v[118:121], v105 offset:3072
	s_cmp_lg_u32 s6, 8
	s_waitcnt lgkmcnt(1)
	v_mov_b32_e32 v192, v110
	s_waitcnt lgkmcnt(0)
	v_mov_b32_e32 v193, v118
	v_mov_b32_e32 v118, v111
	v_pk_mul_f32 v[110:111], v[94:95], v[118:119]
	v_mov_b32_e32 v118, v112
	v_pk_fma_f32 v[110:111], v[98:99], v[192:193], v[110:111]
	v_mov_b32_e32 v119, v120
	v_pk_fma_f32 v[110:111], v[50:51], v[118:119], v[110:111]
	v_mov_b32_e32 v120, v113
	v_pk_fma_f32 v[110:111], v[96:97], v[120:121], v[110:111]
	s_nop 0
	v_add_f32_e32 v108, v108, v110
	v_add_f32_e32 v108, v108, v111
	s_waitcnt lgkmcnt(0)
	s_nop 1
	v_add_f32_dpp v108, v108, v108 quad_perm:[1,0,3,2] row_mask:0xf bank_mask:0xf
	s_nop 1
	v_add_f32_dpp v108, v108, v108 quad_perm:[2,3,0,1] row_mask:0xf bank_mask:0xf
	s_nop 1
	v_add_f32_dpp v108, v108, v108 row_half_mirror row_mask:0xf bank_mask:0xf
	s_nop 1
	v_add_f32_dpp v108, v108, v108 row_mirror row_mask:0xf bank_mask:0xf
	v_mov_b32_e32 v110, v108
	s_nop 1
	v_permlane16_swap_b32_e32 v108, v110
	v_add_f32_e32 v108, v108, v110
	v_mov_b32_e32 v110, v108
	s_nop 1
	v_permlane32_swap_b32_e32 v108, v110
	v_add_f32_e32 v108, v108, v110
	ds_read_b128 v[110:113], v105 offset:4096
	ds_read_b128 v[118:121], v105 offset:5120
	v_cndmask_b32_e32 v106, v106, v108, vcc
	v_cmp_eq_u32_e32 vcc, s7, v147
	s_waitcnt lgkmcnt(1)
	v_mov_b32_e32 v192, v110
	s_waitcnt lgkmcnt(0)
	v_mov_b32_e32 v193, v118
	v_mov_b32_e32 v118, v111
	v_pk_mul_f32 v[110:111], v[48:49], v[118:119]
	v_mov_b32_e32 v118, v112
	v_pk_fma_f32 v[110:111], v[102:103], v[192:193], v[110:111]
	v_mov_b32_e32 v119, v120
	v_pk_fma_f32 v[110:111], v[32:33], v[118:119], v[110:111]
	v_mov_b32_e32 v120, v113
	v_pk_fma_f32 v[110:111], v[100:101], v[120:121], v[110:111]
	s_nop 0
	v_add_f32_e32 v108, 0, v110
	v_add_f32_e32 v108, v108, v111
	ds_read_b128 v[110:113], v105 offset:6144
	ds_read_b128 v[118:121], v105 offset:7168
	v_add_u32_e32 v105, 0x2000, v105
	s_waitcnt lgkmcnt(1)
	v_mov_b32_e32 v192, v110
	s_waitcnt lgkmcnt(0)
	v_mov_b32_e32 v193, v118
	v_mov_b32_e32 v118, v111
	v_pk_mul_f32 v[110:111], v[94:95], v[118:119]
	v_mov_b32_e32 v118, v112
	v_pk_fma_f32 v[110:111], v[98:99], v[192:193], v[110:111]
	v_mov_b32_e32 v119, v120
	v_pk_fma_f32 v[110:111], v[50:51], v[118:119], v[110:111]
	v_mov_b32_e32 v120, v113
	v_pk_fma_f32 v[110:111], v[96:97], v[120:121], v[110:111]
	s_nop 0
	v_add_f32_e32 v108, v108, v110
	v_add_f32_e32 v108, v108, v111
	s_waitcnt lgkmcnt(0)
	s_nop 1
	v_add_f32_dpp v108, v108, v108 quad_perm:[1,0,3,2] row_mask:0xf bank_mask:0xf
	s_nop 1
	v_add_f32_dpp v108, v108, v108 quad_perm:[2,3,0,1] row_mask:0xf bank_mask:0xf
	s_nop 1
	v_add_f32_dpp v108, v108, v108 row_half_mirror row_mask:0xf bank_mask:0xf
	s_nop 1
	v_add_f32_dpp v108, v108, v108 row_mirror row_mask:0xf bank_mask:0xf
	v_mov_b32_e32 v110, v108
	s_nop 1
	v_permlane16_swap_b32_e32 v108, v110
	v_add_f32_e32 v108, v108, v110
	v_mov_b32_e32 v110, v108
	s_nop 1
	v_permlane32_swap_b32_e32 v108, v110
	v_add_f32_e32 v108, v108, v110
	v_cndmask_b32_e32 v106, v106, v108, vcc
	s_cbranch_scc1 .LBB0_93
	s_and_saveexec_b64 s[6:7], s[48:49]
	s_cbranch_execz .LBB0_96
	v_lshlrev_b64 v[32:33], 5, v[190:191]
	v_lshl_add_u64 v[32:33], v[142:143], 0, v[32:33]
	global_store_dword v[32:33], v106, off

; __device__ __forceinline__ f32x4 bf4(const uint2 u) { return (f32x4){__uint_as_float(u.x << 16), __uint_as_float(u.x & 0xffff0000u), __uint_as_float(u.y << 16), __uint_as_float(u.y & 0xffff0000u)}; }
; __device__ __forceinline__ uint2 pack4(const f32x4 v) { uint2 o; o.x = pk2bf(v[0], v[1]); o.y = pk2bf(v[2], v[3]); return o; }
;     template <class T> __device__ __forceinline__ T* w(size_t off) const { return (T*)(p->ws + off); }
; __device__ __forceinline__ void ph_combine(const Ctx& c, int layer, int bid, int G, const int* sm, unsigned char* lds) {
;     ...
;         for (int u = 0; u < 2; ++u) {
;             if (mr[u] != mrc) loadrow(mr[u]);
;             float ss = 0.f;
; #pragma unroll
;             for (int i = 0; i < 4; ++i) { xv[u][i] = xv[u][i] + G2c[i] * (bf4(oa[u][i]) * w0[u] + bf4(ob[u][i]) * w1[u]);
;                 ss += xv[u][i][0] * xv[u][i][0] + xv[u][i][1] * xv[u][i][1] + xv[u][i][2] * xv[u][i][2] + xv[u][i][3] * xv[u][i][3]; }
;             const float rstd = rsqrtf(wave_sum(ss) * (1.f / D) + EPS);
;             if (!ok[u]) continue;
;             const int n = nn[u];
;             if (layer == 1) {
;                 float* o = c.out() + ((size_t)(n / LT) * SEQ + (n % LT - CTX)) * D;
; #pragma unroll
;                 for (int i = 0; i < 4; ++i) { const int k = (lane + 64 * i) * 4; *(f32x4*)(o + k) = xv[u][i] * rstd * GGc[i]; }
;             } else {
;                 float* X = c.w<float>(WS_X) + (size_t)n * D;
;                 f32x4 hv[4];
; #pragma unroll
;                 for (int i = 0; i < 4; ++i) {
;                     const int k = (lane + 64 * i) * 4;
;                     *(f32x4*)(X + k) = xv[u][i];
;                     hv[i] = xv[u][i] * rstd * GGc[i] + SSc[i];
;                     *(uint2*)(HA + (size_t)n * D + k) = pack4(hv[i]);
;                 }
;                 dt_project(wdt, hv, lane, DTR + (size_t)n * 8);
;             }
.LBB0_117:
	s_or_b64 exec, exec, s[28:29]
	s_waitcnt vmcnt(9)
	v_lshlrev_b32_e32 v16, 16, v188
	v_and_b32_e32 v17, 0xffff0000, v188
	v_lshlrev_b32_e32 v12, 16, v186
	v_and_b32_e32 v13, 0xffff0000, v186
	v_pk_mul_f32 v[16:17], v[168:169], v[16:17] op_sel:[1,0]
	s_waitcnt vmcnt(8)
	v_lshlrev_b32_e32 v20, 16, v184
	v_and_b32_e32 v21, 0xffff0000, v184
	v_lshlrev_b32_e32 v18, 16, v189
	v_and_b32_e32 v19, 0xffff0000, v189
	v_pk_fma_f32 v[12:13], v[168:169], v[12:13], v[16:17] op_sel_hi:[0,1,1]
	v_lshlrev_b32_e32 v16, 16, v182
	v_and_b32_e32 v17, 0xffff0000, v182
	v_pk_mul_f32 v[20:21], v[168:169], v[20:21] op_sel:[1,0]
	v_lshlrev_b32_e32 v14, 16, v187
	v_and_b32_e32 v15, 0xffff0000, v187
	v_pk_mul_f32 v[18:19], v[168:169], v[18:19] op_sel:[1,0]
	v_lshlrev_b32_e32 v22, 16, v185
	v_and_b32_e32 v23, 0xffff0000, v185
	v_pk_fma_f32 v[16:17], v[168:169], v[16:17], v[20:21] op_sel_hi:[0,1,1]
	v_pk_fma_f32 v[14:15], v[168:169], v[14:15], v[18:19] op_sel_hi:[0,1,1]
	v_pk_fma_f32 v[12:13], v[12:13], v[54:55], v[90:91]
	v_lshlrev_b32_e32 v18, 16, v183
	v_and_b32_e32 v19, 0xffff0000, v183
	v_pk_mul_f32 v[22:23], v[168:169], v[22:23] op_sel:[1,0]
	v_pk_fma_f32 v[16:17], v[16:17], v[62:63], v[86:87]
	v_pk_fma_f32 v[18:19], v[168:169], v[18:19], v[22:23] op_sel_hi:[0,1,1]
	v_mov_b32_e32 v22, v13
	v_mov_b32_e32 v23, v17
	v_pk_fma_f32 v[14:15], v[14:15], v[56:57], v[92:93]
	v_pk_fma_f32 v[18:19], v[18:19], v[64:65], v[88:89]
	v_mov_b32_e32 v20, v12
	v_mov_b32_e32 v21, v16
	v_pk_mul_f32 v[22:23], v[22:23], v[22:23]
	s_waitcnt vmcnt(7)
	v_lshlrev_b32_e32 v24, 16, v180
	v_pk_fma_f32 v[20:21], v[20:21], v[20:21], v[22:23]
	v_mov_b32_e32 v22, v14
	v_mov_b32_e32 v23, v18
	v_pk_fma_f32 v[20:21], v[22:23], v[22:23], v[20:21]
	v_mov_b32_e32 v22, v15
	v_mov_b32_e32 v23, v19
	v_and_b32_e32 v25, 0xffff0000, v180
	v_pk_fma_f32 v[28:29], v[22:23], v[22:23], v[20:21]
	v_lshlrev_b32_e32 v20, 16, v178
	v_and_b32_e32 v21, 0xffff0000, v178
	v_pk_mul_f32 v[24:25], v[168:169], v[24:25] op_sel:[1,0]
	s_waitcnt vmcnt(6)
	v_lshlrev_b32_e32 v32, 16, v176
	v_and_b32_e32 v33, 0xffff0000, v176
	v_lshlrev_b32_e32 v26, 16, v181
	v_and_b32_e32 v27, 0xffff0000, v181
	v_pk_fma_f32 v[20:21], v[168:169], v[20:21], v[24:25] op_sel_hi:[0,1,1]
	v_lshlrev_b32_e32 v24, 16, v174
	v_and_b32_e32 v25, 0xffff0000, v174
	v_pk_mul_f32 v[32:33], v[168:169], v[32:33] op_sel:[1,0]
	v_lshlrev_b32_e32 v22, 16, v179
	v_and_b32_e32 v23, 0xffff0000, v179
	v_pk_mul_f32 v[26:27], v[168:169], v[26:27] op_sel:[1,0]
	v_lshlrev_b32_e32 v48, 16, v177
	v_and_b32_e32 v49, 0xffff0000, v177
	v_pk_fma_f32 v[24:25], v[168:169], v[24:25], v[32:33] op_sel_hi:[0,1,1]
	v_pk_fma_f32 v[22:23], v[168:169], v[22:23], v[26:27] op_sel_hi:[0,1,1]
	v_pk_fma_f32 v[20:21], v[20:21], v[70:71], v[82:83]
	v_lshlrev_b32_e32 v26, 16, v175
	v_and_b32_e32 v27, 0xffff0000, v175
	v_pk_mul_f32 v[48:49], v[168:169], v[48:49] op_sel:[1,0]
	v_pk_fma_f32 v[24:25], v[24:25], v[4:5], v[78:79]
	v_pk_fma_f32 v[26:27], v[168:169], v[26:27], v[48:49] op_sel_hi:[0,1,1]
	v_mov_b32_e32 v48, v21
	v_mov_b32_e32 v49, v25
	v_pk_fma_f32 v[22:23], v[22:23], v[72:73], v[84:85]
	v_pk_fma_f32 v[26:27], v[26:27], v[6:7], v[80:81]
	v_mov_b32_e32 v32, v20
	v_mov_b32_e32 v33, v24
	v_pk_mul_f32 v[48:49], v[48:49], v[48:49]
	v_add_f32_e32 v28, v28, v29
	v_pk_fma_f32 v[32:33], v[32:33], v[32:33], v[48:49]
	v_mov_b32_e32 v48, v22
	v_mov_b32_e32 v49, v26
	v_pk_fma_f32 v[32:33], v[48:49], v[48:49], v[32:33]
	v_mov_b32_e32 v48, v23
	v_mov_b32_e32 v49, v27
	v_pk_fma_f32 v[32:33], v[48:49], v[48:49], v[32:33]
	v_cmp_gt_i32_e32 vcc, s55, v155
	v_add_f32_e32 v28, v28, v32
	v_add_f32_e32 v28, v28, v33
	s_waitcnt lgkmcnt(0)
	s_nop 1
	v_add_f32_dpp v28, v28, v28 quad_perm:[1,0,3,2] row_mask:0xf bank_mask:0xf
	s_nop 1
	v_add_f32_dpp v28, v28, v28 quad_perm:[2,3,0,1] row_mask:0xf bank_mask:0xf
	s_nop 1
	v_add_f32_dpp v28, v28, v28 row_half_mirror row_mask:0xf bank_mask:0xf
	s_nop 1
	v_add_f32_dpp v28, v28, v28 row_mirror row_mask:0xf bank_mask:0xf
	v_mov_b32_e32 v29, v28
	s_nop 1
	v_permlane16_swap_b32_e32 v28, v29
	v_add_f32_e32 v28, v28, v29
	v_mov_b32_e32 v29, v28
	s_nop 1
	v_permlane32_swap_b32_e32 v28, v29
	v_add_f32_e32 v28, v28, v29
	s_and_saveexec_b64 s[28:29], vcc
	s_cbranch_execz .LBB0_64
	v_fmamk_f32 v28, v28, 0x3a800000, v220
	v_mul_f32_e32 v29, 0x4b800000, v28
	v_cmp_gt_f32_e64 s[50:51], s91, v28
	s_and_b64 vcc, exec, s[46:47]
	s_mov_b64 s[6:7], -1
	v_cndmask_b32_e64 v28, v28, v29, s[50:51]
	v_rsq_f32_e32 v28, v28
	s_nop 0
	v_mul_f32_e32 v29, 0x45800000, v28
	v_cndmask_b32_e64 v28, v28, v29, s[50:51]
	s_cbranch_vccnz .LBB0_124
	v_pk_mul_f32 v[32:33], v[14:15], v[28:29] op_sel_hi:[1,0]
	v_pk_mul_f32 v[48:49], v[12:13], v[28:29] op_sel_hi:[1,0]
	v_pk_fma_f32 v[32:33], v[36:37], v[32:33], v[60:61]
	v_pk_fma_f32 v[88:89], v[38:39], v[48:49], v[58:59]
	v_lshlrev_b64 v[50:51], 11, v[164:165]
	v_cvt_pk_bf16_f32 v48, v88, v89
	v_cvt_pk_bf16_f32 v49, v32, v33
	v_lshl_add_u64 v[80:81], v[162:163], 0, v[50:51]
	global_store_dwordx4 v[172:173], v[12:15], off
	global_store_dwordx2 v[80:81], v[48:49], off
	global_store_dwordx4 v[172:173], v[16:19], off offset:1024
	v_pk_mul_f32 v[48:49], v[18:19], v[28:29] op_sel_hi:[1,0]
	v_pk_mul_f32 v[50:51], v[16:17], v[28:29] op_sel_hi:[1,0]
	v_pk_fma_f32 v[86:87], v[40:41], v[48:49], v[68:69]
	v_pk_fma_f32 v[48:49], v[42:43], v[50:51], v[66:67]
	v_cvt_pk_bf16_f32 v51, v86, v87
	v_cvt_pk_bf16_f32 v50, v48, v49
	global_store_dwordx2 v[80:81], v[50:51], off offset:512
	global_store_dwordx4 v[172:173], v[20:23], off offset:2048
	v_pk_mul_f32 v[50:51], v[22:23], v[28:29] op_sel_hi:[1,0]
	v_pk_mul_f32 v[78:79], v[20:21], v[28:29] op_sel_hi:[1,0]
	v_pk_fma_f32 v[50:51], v[30:31], v[50:51], v[76:77]
	v_pk_fma_f32 v[84:85], v[44:45], v[78:79], v[74:75]
	v_cvt_pk_bf16_f32 v79, v50, v51
	v_cvt_pk_bf16_f32 v78, v84, v85
	global_store_dwordx2 v[80:81], v[78:79], off offset:1024
	global_store_dwordx4 v[172:173], v[24:27], off offset:3072
	v_pk_mul_f32 v[78:79], v[26:27], v[28:29] op_sel_hi:[1,0]
	v_pk_mul_f32 v[82:83], v[24:25], v[28:29] op_sel_hi:[1,0]
	v_pk_fma_f32 v[90:91], v[34:35], v[78:79], v[10:11]
	v_pk_fma_f32 v[78:79], v[46:47], v[82:83], v[8:9]
	v_cvt_pk_bf16_f32 v83, v90, v91
	v_cvt_pk_bf16_f32 v82, v78, v79
	global_store_dwordx2 v[80:81], v[82:83], off offset:1536
	v_mov_b32_e32 v80, v51
	v_mov_b32_e32 v81, v91
	v_mov_b32_e32 v51, v90
	v_mov_b32_e32 v82, v84
	v_mov_b32_e32 v83, v78
	v_mov_b32_e32 v78, v85
	v_mov_b32_e32 v84, v33
	v_mov_b32_e32 v85, v87
	v_mov_b32_e32 v33, v86
	v_mov_b32_e32 v86, v88
	v_mov_b32_e32 v87, v48
	v_mov_b32_e32 v48, v89
	s_mov_b32 s6, 0
	v_mov_b32_e32 v89, 0
	v_mov_b32_e32 v29, v147
	v_mov_b32_e32 v88, v149
; #define LAS __attribute__((address_space(3)))
;     template <class T> __device__ __forceinline__ T* w(size_t off) const { return (T*)(p->ws + off); }
; __device__ __forceinline__ void dt_project(const LAS float* wdt, const f32x4 (&h)[4], int lane, float* dst) {
;     float mine = 0.f;
; #pragma unroll 2
;     for (int q = 0; q < 8; ++q) {
;         float s = 0.f;
; #pragma unroll
;         for (int i = 0; i < 4; ++i) { const f32x4 w = *(const LAS f32x4*)(wdt + q * 1024 + (lane + 64 * i) * 4); s += h[i][0] * w[0] + h[i][1] * w[1] + h[i][2] * w[2] + h[i][3] * w[3]; }
;         s = wave_sum(s);
;         if (lane == q) mine = s;
;     }
;     if (lane < 8) dst[lane] = mine;
; }
.LBB0_120:
	ds_read_b128 v[90:93], v88
	ds_read_b128 v[94:97], v88 offset:1024
	v_cmp_eq_u32_e32 vcc, 0, v29
	s_or_b32 s7, s6, 1
	s_add_i32 s6, s6, 2
	s_waitcnt lgkmcnt(1)
	v_mov_b32_e32 v98, v90
	s_waitcnt lgkmcnt(0)
	v_mov_b32_e32 v99, v94
	v_mov_b32_e32 v94, v91
	v_pk_mul_f32 v[90:91], v[48:49], v[94:95]
	v_mov_b32_e32 v94, v92
	v_pk_fma_f32 v[90:91], v[86:87], v[98:99], v[90:91]
	v_mov_b32_e32 v95, v96
	v_pk_fma_f32 v[90:91], v[32:33], v[94:95], v[90:91]
	v_mov_b32_e32 v96, v93
	v_pk_fma_f32 v[90:91], v[84:85], v[96:97], v[90:91]
	v_add_u32_e32 v29, -2, v29
	v_add_f32_e32 v90, 0, v90
	v_add_f32_e32 v100, v90, v91
	ds_read_b128 v[90:93], v88 offset:2048
	ds_read_b128 v[94:97], v88 offset:3072
	s_cmp_lg_u32 s6, 8
	s_waitcnt lgkmcnt(1)
	v_mov_b32_e32 v98, v90
	s_waitcnt lgkmcnt(0)
	v_mov_b32_e32 v99, v94
	v_mov_b32_e32 v94, v91
	v_pk_mul_f32 v[90:91], v[78:79], v[94:95]
	v_mov_b32_e32 v94, v92
	v_pk_fma_f32 v[90:91], v[82:83], v[98:99], v[90:91]
	v_mov_b32_e32 v95, v96
	v_pk_fma_f32 v[90:91], v[50:51], v[94:95], v[90:91]
	v_mov_b32_e32 v96, v93
	v_pk_fma_f32 v[90:91], v[80:81], v[96:97], v[90:91]
	s_nop 0
	v_add_f32_e32 v90, v100, v90
	v_add_f32_e32 v90, v90, v91
	s_waitcnt lgkmcnt(0)
	s_nop 1
	v_add_f32_dpp v90, v90, v90 quad_perm:[1,0,3,2] row_mask:0xf bank_mask:0xf
	s_nop 1
	v_add_f32_dpp v90, v90, v90 quad_perm:[2,3,0,1] row_mask:0xf bank_mask:0xf
	s_nop 1
	v_add_f32_dpp v90, v90, v90 row_half_mirror row_mask:0xf bank_mask:0xf
	s_nop 1
	v_add_f32_dpp v90, v90, v90 row_mirror row_mask:0xf bank_mask:0xf
	v_mov_b32_e32 v91, v90
	s_nop 1
	v_permlane16_swap_b32_e32 v90, v91
	v_add_f32_e32 v90, v90, v91
	v_mov_b32_e32 v91, v90
	s_nop 1
	v_permlane32_swap_b32_e32 v90, v91
	v_add_f32_e32 v90, v90, v91
	v_cndmask_b32_e32 v89, v89, v90, vcc
	ds_read_b128 v[90:93], v88 offset:4096
	ds_read_b128 v[94:97], v88 offset:5120
	v_cmp_eq_u32_e32 vcc, s7, v147
	s_waitcnt lgkmcnt(1)
	v_mov_b32_e32 v98, v90
	s_waitcnt lgkmcnt(0)
	v_mov_b32_e32 v99, v94
	v_mov_b32_e32 v94, v91
	v_pk_mul_f32 v[90:91], v[48:49], v[94:95]
	v_mov_b32_e32 v94, v92
	v_pk_fma_f32 v[90:91], v[86:87], v[98:99], v[90:91]
	v_mov_b32_e32 v95, v96
	v_pk_fma_f32 v[90:91], v[32:33], v[94:95], v[90:91]
	v_mov_b32_e32 v96, v93
	v_pk_fma_f32 v[90:91], v[84:85], v[96:97], v[90:91]
	s_nop 0
	v_add_f32_e32 v90, 0, v90
	v_add_f32_e32 v100, v90, v91
	ds_read_b128 v[90:93], v88 offset:6144
	ds_read_b128 v[94:97], v88 offset:7168
	v_add_u32_e32 v88, 0x2000, v88
	s_waitcnt lgkmcnt(1)
	v_mov_b32_e32 v98, v90
	s_waitcnt lgkmcnt(0)
	v_mov_b32_e32 v99, v94
	v_mov_b32_e32 v94, v91
	v_pk_mul_f32 v[90:91], v[78:79], v[94:95]
	v_mov_b32_e32 v94, v92
	v_pk_fma_f32 v[90:91], v[82:83], v[98:99], v[90:91]
	v_mov_b32_e32 v95, v96
	v_pk_fma_f32 v[90:91], v[50:51], v[94:95], v[90:91]
	v_mov_b32_e32 v96, v93
	v_pk_fma_f32 v[90:91], v[80:81], v[96:97], v[90:91]
	s_nop 0
	v_add_f32_e32 v90, v100, v90
	v_add_f32_e32 v90, v90, v91
	s_waitcnt lgkmcnt(0)
	s_nop 1
	v_add_f32_dpp v90, v90, v90 quad_perm:[1,0,3,2] row_mask:0xf bank_mask:0xf
	s_nop 1
	v_add_f32_dpp v90, v90, v90 quad_perm:[2,3,0,1] row_mask:0xf bank_mask:0xf
	s_nop 1
	v_add_f32_dpp v90, v90, v90 row_half_mirror row_mask:0xf bank_mask:0xf
	s_nop 1
	v_add_f32_dpp v90, v90, v90 row_mirror row_mask:0xf bank_mask:0xf
	v_mov_b32_e32 v91, v90
	s_nop 1
	v_permlane16_swap_b32_e32 v90, v91
	v_add_f32_e32 v90, v90, v91
	v_mov_b32_e32 v91, v90
	s_nop 1
	v_permlane32_swap_b32_e32 v90, v91
	v_add_f32_e32 v90, v90, v91
	v_cndmask_b32_e32 v89, v89, v90, vcc
	s_cbranch_scc1 .LBB0_120
	s_and_saveexec_b64 s[6:7], s[48:49]
	s_cbranch_execz .LBB0_123
	v_lshlrev_b64 v[32:33], 5, v[164:165]
	v_lshl_add_u64 v[32:33], v[142:143], 0, v[32:33]
	global_store_dword v[32:33], v89, off
